# P + attention: K fragments for the next MFMA segment prefetched at the tail of the previous MFMA segment into spare VGPRs v222-253 (removed from the softmax segment's tail)
# baseline (speedup 1.0000x reference)
.LBB0_1608:
	s_and_b32 s2, s4, 0x3fffffc0
	s_lshl_b32 s2, s2, 2
	s_add_i32 s13, s2, 0
	v_and_b32_e32 v193, 63, v192
	v_exp_f32_e32 v159, v81
	v_exp_f32_e32 v167, v97
	v_exp_f32_e32 v158, v80
	v_exp_f32_e32 v156, v82
	v_exp_f32_e32 v157, v83
	v_exp_f32_e32 v166, v96
	v_exp_f32_e32 v164, v98
	v_exp_f32_e32 v165, v99
	v_exp_f32_e32 v154, v84
	v_exp_f32_e32 v155, v85
	v_exp_f32_e32 v162, v100
	v_exp_f32_e32 v163, v101
	v_exp_f32_e32 v152, v86
	v_exp_f32_e32 v153, v87
	v_exp_f32_e32 v160, v102
	v_exp_f32_e32 v161, v103
	v_exp_f32_e32 v150, v88
	v_exp_f32_e32 v151, v89
	v_exp_f32_e32 v104, v104
	v_exp_f32_e32 v105, v105
	v_max_f32_e32 v65, v159, v167
	v_exp_f32_e32 v148, v90
	v_exp_f32_e32 v149, v91
	v_exp_f32_e32 v102, v106
	v_exp_f32_e32 v103, v107
	v_max3_f32 v65, v158, v166, v65
	v_max_f32_e32 v66, v156, v164
	v_max_f32_e32 v67, v157, v165
	v_exp_f32_e32 v146, v92
	v_exp_f32_e32 v147, v93
	v_exp_f32_e32 v100, v108
	v_exp_f32_e32 v101, v109
	v_max3_f32 v65, v65, v66, v67
	v_max_f32_e32 v66, v154, v162
	v_max_f32_e32 v67, v155, v163
	v_exp_f32_e32 v144, v94
	v_exp_f32_e32 v145, v95
	v_exp_f32_e32 v98, v110
	v_exp_f32_e32 v99, v111
	v_max3_f32 v65, v65, v66, v67
	v_max_f32_e32 v66, v152, v160
	v_max_f32_e32 v67, v153, v161
	v_max3_f32 v65, v65, v66, v67
	v_max_f32_e32 v66, v150, v104
	v_max_f32_e32 v67, v151, v105
	v_max3_f32 v65, v65, v66, v67
	v_max_f32_e32 v66, v148, v102
	v_max_f32_e32 v67, v149, v103
	v_max3_f32 v65, v65, v66, v67
	v_max_f32_e32 v66, v146, v100
	v_max_f32_e32 v67, v147, v101
	v_max3_f32 v65, v65, v66, v67
	v_max_f32_e32 v66, v144, v98
	v_max_f32_e32 v67, v145, v99
	v_max3_f32 v65, v65, v66, v67
	v_mov_b32_e32 v66, v65
	s_nop 1
	v_permlane32_swap_b32_e32 v65, v66
	v_max_f32_e32 v66, v66, v66
	v_max_f32_e32 v65, v65, v65
	v_max_f32_e32 v65, v65, v66
	v_log_f32_e32 v65, v65
	v_cmp_gt_u32_e64 s[2:3], 32, v193
	v_lshl_add_u32 v196, v194, 2, s13
	v_add_f32_e32 v65, 0xc0400000, v65
	v_max_f32_e32 v65, 0, v65
	v_ceil_f32_e32 v65, v65
	v_exp_f32_e64 v106, -v65
	s_and_saveexec_b64 s[4:5], s[2:3]
	ds_write_b32 v196, v106 offset:60544
	s_or_b64 exec, exec, s[4:5]
	v_pk_mul_f32 v[66:67], v[158:159], v[106:107] op_sel_hi:[1,0]
	v_pk_mul_f32 v[82:83], v[166:167], v[106:107] op_sel_hi:[1,0]
	v_pk_mul_f32 v[68:69], v[156:157], v[106:107] op_sel_hi:[1,0]
	v_pk_mul_f32 v[84:85], v[164:165], v[106:107] op_sel_hi:[1,0]
	v_pk_mul_f32 v[70:71], v[154:155], v[106:107] op_sel_hi:[1,0]
	v_pk_mul_f32 v[86:87], v[162:163], v[106:107] op_sel_hi:[1,0]
	v_pk_mul_f32 v[72:73], v[152:153], v[106:107] op_sel_hi:[1,0]
	v_pk_mul_f32 v[88:89], v[160:161], v[106:107] op_sel_hi:[1,0]
	v_pk_mul_f32 v[74:75], v[150:151], v[106:107] op_sel_hi:[1,0]
	v_pk_mul_f32 v[90:91], v[104:105], v[106:107] op_sel_hi:[1,0]
	v_pk_mul_f32 v[76:77], v[148:149], v[106:107] op_sel_hi:[1,0]
	v_pk_mul_f32 v[92:93], v[102:103], v[106:107] op_sel_hi:[1,0]
	v_pk_mul_f32 v[78:79], v[146:147], v[106:107] op_sel_hi:[1,0]
	v_pk_mul_f32 v[94:95], v[100:101], v[106:107] op_sel_hi:[1,0]
	v_pk_mul_f32 v[80:81], v[144:145], v[106:107] op_sel_hi:[1,0]
	v_pk_mul_f32 v[96:97], v[98:99], v[106:107] op_sel_hi:[1,0]
	v_add_f32_e32 v107, 0, v158
	v_add_f32_e32 v107, v159, v107
	v_add_f32_e32 v107, v156, v107
	v_add_f32_e32 v107, v157, v107
	v_add_f32_e32 v107, v154, v107
	v_add_f32_e32 v107, v155, v107
	v_add_f32_e32 v107, v152, v107
	v_add_f32_e32 v107, v153, v107
	v_add_f32_e32 v107, v150, v107
	v_add_f32_e32 v107, v151, v107
	v_add_f32_e32 v107, v148, v107
	v_add_f32_e32 v107, v149, v107
	v_add_f32_e32 v107, v146, v107
	v_add_f32_e32 v107, v147, v107
	v_add_f32_e32 v107, v144, v107
	v_add_f32_e32 v107, v145, v107
	v_add_f32_e32 v107, v166, v107
	v_add_f32_e32 v107, v167, v107
	v_add_f32_e32 v107, v164, v107
	v_add_f32_e32 v107, v165, v107
	v_add_f32_e32 v107, v162, v107
	v_add_f32_e32 v107, v163, v107
	v_add_f32_e32 v107, v160, v107
	v_add_f32_e32 v107, v161, v107
	v_add_f32_e32 v104, v104, v107
	v_add_f32_e32 v104, v105, v104
	v_add_f32_e32 v102, v102, v104
	v_add_f32_e32 v102, v103, v102
	v_add_f32_e32 v100, v100, v102
	v_add_f32_e32 v100, v101, v100
	v_add_f32_e32 v98, v98, v100
	v_lshrrev_b32_e32 v100, 3, v192
	v_and_b32_e32 v195, 4, v100
	s_waitcnt lgkmcnt(0)
	v_lshl_add_u32 v197, v195, 2, s13
	ds_read_b128 v[100:103], v197 offset:60608
	ds_read_b128 v[108:111], v197 offset:60640
	ds_read_b128 v[206:209], v197 offset:60544
	ds_read_b128 v[144:147], v197 offset:60576
	v_cvt_pk_fp8_f32 v112, v66, v67
	v_cvt_pk_fp8_f32 v113, v70, v71
	v_cvt_pk_fp8_f32 v114, v74, v75
	v_cvt_pk_fp8_f32 v115, v78, v79
	s_waitcnt lgkmcnt(0)
	v_pk_mul_f32 v[4:5], v[4:5], v[144:145]
	v_pk_mul_f32 v[6:7], v[6:7], v[146:147]
	v_pk_mul_f32 v[20:21], v[20:21], v[144:145]
	v_pk_mul_f32 v[22:23], v[22:23], v[146:147]
	v_pk_mul_f32 v[36:37], v[36:37], v[144:145]
	v_pk_mul_f32 v[38:39], v[38:39], v[146:147]
	v_pk_mul_f32 v[52:53], v[52:53], v[144:145]
	v_pk_mul_f32 v[54:55], v[54:55], v[146:147]
	ds_read_b128 v[222:225], v204 offset:33792
	ds_read_b128 v[226:229], v204 offset:33808
	ds_read_b128 v[230:233], v204 offset:40448
	ds_read_b128 v[234:237], v204 offset:40464
	ds_read_b128 v[238:241], v204 offset:33856
	ds_read_b128 v[242:245], v204 offset:33872
	ds_read_b128 v[246:249], v204 offset:40512
	ds_read_b128 v[250:253], v204 offset:40528
	v_cvt_pk_fp8_f32 v116, v82, v83
	v_cvt_pk_fp8_f32 v117, v86, v87
	v_cvt_pk_fp8_f32 v118, v90, v91
	v_cvt_pk_fp8_f32 v119, v94, v95
	v_cvt_pk_fp8_f32 v112, v68, v69 op_sel:[0,0,1]
	v_cvt_pk_fp8_f32 v113, v72, v73 op_sel:[0,0,1]
	v_cvt_pk_fp8_f32 v114, v76, v77 op_sel:[0,0,1]
	v_cvt_pk_fp8_f32 v115, v80, v81 op_sel:[0,0,1]
	v_cvt_pk_fp8_f32 v116, v84, v85 op_sel:[0,0,1]
	v_cvt_pk_fp8_f32 v117, v88, v89 op_sel:[0,0,1]
	v_cvt_pk_fp8_f32 v118, v92, v93 op_sel:[0,0,1]
	v_cvt_pk_fp8_f32 v119, v96, v97 op_sel:[0,0,1]
	v_mul_f32_e32 v187, 0, v106
	v_add_f32_e32 v98, v99, v98
	v_pk_mul_f32 v[12:13], v[12:13], v[108:109]
	v_pk_mul_f32 v[8:9], v[8:9], v[100:101]
	v_pk_mul_f32 v[14:15], v[14:15], v[110:111]
	v_pk_mul_f32 v[10:11], v[10:11], v[102:103]
	v_pk_mul_f32 v[2:3], v[2:3], v[208:209]
	v_pk_mul_f32 v[0:1], v[0:1], v[206:207]
	v_pk_mul_f32 v[28:29], v[28:29], v[108:109]
	v_pk_mul_f32 v[24:25], v[24:25], v[100:101]
	v_pk_mul_f32 v[30:31], v[30:31], v[110:111]
	v_pk_mul_f32 v[26:27], v[26:27], v[102:103]
	v_pk_mul_f32 v[18:19], v[18:19], v[208:209]
	v_pk_mul_f32 v[16:17], v[16:17], v[206:207]
	v_pk_mul_f32 v[44:45], v[44:45], v[108:109]
	v_pk_mul_f32 v[40:41], v[40:41], v[100:101]
	v_pk_mul_f32 v[46:47], v[46:47], v[110:111]
	v_pk_mul_f32 v[42:43], v[42:43], v[102:103]
	v_pk_mul_f32 v[34:35], v[34:35], v[208:209]
	v_pk_mul_f32 v[32:33], v[32:33], v[206:207]
	v_pk_mul_f32 v[60:61], v[60:61], v[108:109]
	v_pk_mul_f32 v[56:57], v[56:57], v[100:101]
	v_pk_mul_f32 v[62:63], v[62:63], v[110:111]
	v_pk_mul_f32 v[58:59], v[58:59], v[102:103]
	v_pk_mul_f32 v[50:51], v[50:51], v[208:209]
	v_pk_mul_f32 v[48:49], v[48:49], v[206:207]
	v_mul_f32_e32 v98, v98, v106
	v_add_f32_e32 v187, v187, v98
	s_nop 0
	v_cndmask_b32_e64 v66, 0, 1, s[6:7]
	v_cmp_ne_u32_e64 s[4:5], 1, v66
	s_andn2_b64 vcc, exec, s[6:7]
	s_cbranch_vccnz .LBB0_1612
	s_waitcnt lgkmcnt(0)
	s_barrier

.LBB0_1614:
	s_mul_i32 s14, s13, 0x3400
	s_and_b32 s7, 1, s18
	s_add_i32 s14, s14, 0
	s_andn2_b32 s15, 1, s18
	s_mul_i32 s6, s17, 0x3400
	s_cmpk_lt_u32 s18, 0xfc
	s_cselect_b32 s21, s20, 0x2fd000
	s_cmp_eq_u32 s7, 1
	v_add_u32_e32 v96, s14, v199
	s_waitcnt lgkmcnt(6)
	v_mfma_scale_f32_32x32x64_f8f6f4 v[80:95], v[222:229], v[136:143], v[64:79], v191, v190 op_sel_hi:[0,0,0]
	s_waitcnt vmcnt(2)
	ds_write_b128 v96, v[180:183] offset:20480
	v_add_u32_e32 v96, s14, v200
	s_mulk_i32 s15, 0x2800
	s_waitcnt vmcnt(1)
	ds_write_b64 v96, v[188:189] offset:28672
	v_add_u32_e32 v96, s15, v205
	s_mov_b32 s39, s31
	s_waitcnt vmcnt(0)
	ds_write_b128 v96, v[176:179]
	buffer_load_dwordx4 v[180:183], v203, s[28:31], s21 offen
	buffer_load_dwordx2 v[188:189], v202, s[28:31], s21 offen
	buffer_load_dwordx4 v[176:179], v203, s[36:39], s19 offen
	v_add_u32_e32 v172, s6, v204
	s_cselect_b32 s6, 0x2800, 0
	v_add_u32_e32 v186, s6, v198
	s_waitcnt lgkmcnt(7)
	v_mfma_scale_f32_32x32x64_f8f6f4 v[96:111], v[230:237], v[136:143], v[64:79], v191, v190 op_sel_hi:[0,0,0]
	ds_read_b128 v[160:163], v172 offset:20608
	ds_read_b128 v[164:167], v172 offset:20624
	ds_read_b128 v[168:171], v172 offset:27264
	ds_read_b128 v[172:175], v172 offset:27280
	s_waitcnt lgkmcnt(9)
	v_mfma_scale_f32_32x32x64_f8f6f4 v[80:95], v[238:245], v[128:135], v[80:95], v191, v190 op_sel_hi:[0,0,0]
	ds_read_b128 v[152:155], v186
	ds_read_b128 v[156:159], v186 offset:16
	ds_read_b128 v[206:209], v186 offset:2560
	ds_read_b128 v[210:213], v186 offset:2576
	s_waitcnt lgkmcnt(11)
	v_mfma_scale_f32_32x32x64_f8f6f4 v[96:111], v[246:253], v[128:135], v[96:111], v191, v190 op_sel_hi:[0,0,0]
	ds_read_b128 v[144:147], v186 offset:5120
	ds_read_b128 v[148:151], v186 offset:5136
	ds_read_b128 v[214:217], v186 offset:7680
	ds_read_b128 v[218:221], v186 offset:7696
	s_waitcnt lgkmcnt(10)
	v_mfma_scale_f32_32x32x64_f8f6f4 v[80:95], v[160:167], v[120:127], v[80:95], v191, v190 op_sel_hi:[0,0,0]
	s_waitcnt lgkmcnt(8)
	v_mfma_scale_f32_32x32x64_f8f6f4 v[96:111], v[168:175], v[120:127], v[96:111], v191, v190 op_sel_hi:[0,0,0]
	s_waitcnt lgkmcnt(6)
	v_mfma_f32_32x32x64_f8f6f4 v[0:15], v[112:119], v[152:159], v[0:15]
	s_waitcnt lgkmcnt(4)
	v_mfma_f32_32x32x64_f8f6f4 v[16:31], v[112:119], v[206:213], v[16:31]
	s_waitcnt lgkmcnt(2)
	v_mfma_f32_32x32x64_f8f6f4 v[32:47], v[112:119], v[144:151], v[32:47]
	s_waitcnt lgkmcnt(0)
	v_mfma_f32_32x32x64_f8f6f4 v[48:63], v[112:119], v[214:221], v[48:63]
	s_mul_i32 s14, s16, 0x3400
	v_add_u32_e32 v254, s14, v204
	ds_read_b128 v[222:225], v254 offset:20480
	ds_read_b128 v[226:229], v254 offset:20496
	ds_read_b128 v[230:233], v254 offset:27136
	ds_read_b128 v[234:237], v254 offset:27152
	ds_read_b128 v[238:241], v254 offset:20544
	ds_read_b128 v[242:245], v254 offset:20560
	ds_read_b128 v[246:249], v254 offset:27200
	ds_read_b128 v[250:253], v254 offset:27216
	v_cndmask_b32_e64 v144, 0, 1, s[46:47]
	v_cmp_ne_u32_e64 s[6:7], 1, v144
	s_andn2_b64 vcc, exec, s[46:47]
	s_cbranch_vccnz .LBB0_1616
	s_barrier

.LBB0_1617:
	v_cvt_pk_fp8_f32 v112, v80, v81
	v_cvt_pk_fp8_f32 v113, v84, v85
	v_cvt_pk_fp8_f32 v114, v88, v89
	v_cvt_pk_fp8_f32 v115, v92, v93
	v_cvt_pk_fp8_f32 v116, v96, v97
	v_cvt_pk_fp8_f32 v117, v100, v101
	v_cvt_pk_fp8_f32 v118, v104, v105
	v_cvt_pk_fp8_f32 v119, v108, v109
	v_cvt_pk_fp8_f32 v112, v82, v83 op_sel:[0,0,1]
	v_cvt_pk_fp8_f32 v113, v86, v87 op_sel:[0,0,1]
	v_cvt_pk_fp8_f32 v114, v90, v91 op_sel:[0,0,1]
	v_cvt_pk_fp8_f32 v115, v94, v95 op_sel:[0,0,1]
	v_cvt_pk_fp8_f32 v116, v98, v99 op_sel:[0,0,1]
	v_cvt_pk_fp8_f32 v117, v102, v103 op_sel:[0,0,1]
	v_cvt_pk_fp8_f32 v118, v106, v107 op_sel:[0,0,1]
	v_cvt_pk_fp8_f32 v119, v110, v111 op_sel:[0,0,1]
	v_add_f32_e32 v187, v187, v186
	s_nop 0
	s_and_b64 vcc, exec, s[4:5]
	s_cbranch_vccnz .LBB0_1613
	s_waitcnt lgkmcnt(0)
	s_barrier
	s_branch .LBB0_1613

.LBB0_1622:
	s_mul_i32 s14, s17, 0x3400
	s_mulk_i32 s13, 0x3400
	s_add_i32 s13, s13, 0
	v_add_u32_e32 v96, s13, v199
	s_waitcnt lgkmcnt(6)
	v_mfma_scale_f32_32x32x64_f8f6f4 v[80:95], v[222:229], v[136:143], v[64:79], v191, v190 op_sel_hi:[0,0,0]
	s_waitcnt vmcnt(2)
	ds_write_b128 v96, v[180:183] offset:20480
	v_add_u32_e32 v96, s13, v200
	s_waitcnt vmcnt(1)
	ds_write_b64 v96, v[188:189] offset:28672
	s_waitcnt vmcnt(0)
	ds_write_b128 v205, v[176:179] offset:10240
	v_add3_u32 v108, v201, s14, v184
	s_waitcnt lgkmcnt(7)
	v_mfma_scale_f32_32x32x64_f8f6f4 v[64:79], v[230:237], v[136:143], v[64:79], v191, v190 op_sel_hi:[0,0,0]
	ds_read_b128 v[96:99], v108 offset:20608
	ds_read_b128 v[100:103], v108 offset:20624
	ds_read_b128 v[104:107], v108 offset:27264
	ds_read_b128 v[108:111], v108 offset:27280
	s_waitcnt lgkmcnt(9)
	v_mfma_scale_f32_32x32x64_f8f6f4 v[80:95], v[238:245], v[128:135], v[80:95], v191, v190 op_sel_hi:[0,0,0]
	ds_read_b128 v[136:139], v198
	ds_read_b128 v[140:143], v198 offset:16
	ds_read_b128 v[152:155], v198 offset:2560
	ds_read_b128 v[156:159], v198 offset:2576
	s_waitcnt lgkmcnt(11)
	v_mfma_scale_f32_32x32x64_f8f6f4 v[64:79], v[246:253], v[128:135], v[64:79], v191, v190 op_sel_hi:[0,0,0]
	ds_read_b128 v[128:131], v198 offset:5120
	ds_read_b128 v[132:135], v198 offset:5136
	ds_read_b128 v[144:147], v198 offset:7680
	ds_read_b128 v[148:151], v198 offset:7696
	s_waitcnt lgkmcnt(10)
	v_mfma_scale_f32_32x32x64_f8f6f4 v[80:95], v[96:103], v[120:127], v[80:95], v191, v190 op_sel_hi:[0,0,0]
	s_waitcnt lgkmcnt(8)
	v_mfma_scale_f32_32x32x64_f8f6f4 v[64:79], v[104:111], v[120:127], v[64:79], v191, v190 op_sel_hi:[0,0,0]
	s_waitcnt lgkmcnt(6)
	v_mfma_f32_32x32x64_f8f6f4 v[0:15], v[112:119], v[136:143], v[0:15]
	s_waitcnt lgkmcnt(4)
	v_mfma_f32_32x32x64_f8f6f4 v[16:31], v[112:119], v[152:159], v[16:31]
	s_waitcnt lgkmcnt(2)
	v_mfma_f32_32x32x64_f8f6f4 v[32:47], v[112:119], v[128:135], v[32:47]
	s_waitcnt lgkmcnt(0)
	v_mfma_f32_32x32x64_f8f6f4 v[48:63], v[112:119], v[144:151], v[48:63]
	s_and_b64 vcc, exec, s[6:7]
	s_cbranch_vccnz .LBB0_1624
	s_barrier
